# attention tile loop rewritten by hand: ping-pong halves, V fragments prefetched into K-fragment registers, K(t+1) fragment reads interleaved with PV MFMAs
# speedup vs baseline: 1.0073x; 1.0073x over previous
.LBB0_1088:
	v_lshlrev_b32_e32 v13, 3, v146
	v_and_b32_e32 v12, 0xc0, v12
	v_lshlrev_b32_e32 v14, 1, v146
	s_xor_b64 s[34:35], s[4:5], -1
	v_and_or_b32 v12, v13, 24, v12
	v_and_b32_e32 v14, 32, v14
	v_and_b32_e32 v13, 0x100, v13
	s_add_i32 s44, s44, s8
	v_or3_b32 v12, v12, v14, v13
	v_or_b32_e32 v13, s44, v145
	s_cmp_lg_u32 0, -1
	s_cselect_b32 s4, 0, 0
	s_lshr_b32 s46, s7, 6
	v_add_u32_e32 v163, 0xffffff91, v13
	v_lshlrev_b32_e32 v164, 4, v4
	v_lshlrev_b32_e32 v13, 4, v145
	s_add_i32 s38, 0, 0x10800
	s_add_i32 s47, s46, -2
	s_or_b32 s64, s44, 31
	v_and_b32_e32 v13, 0x70, v13
	v_add_u32_e32 v14, 32, v164
	v_lshl_add_u32 v171, v146, 2, s38
	s_lshl_b32 s38, s46, 8
	v_xad_u32 v168, v14, v13, 0
	v_add_u32_e32 v14, 64, v164
	s_add_u32 s38, s89, s38
	v_xad_u32 v169, v14, v13, 0
	v_add_u32_e32 v14, 0x60, v164
	s_addc_u32 s39, s88, 0
	s_and_b32 s7, s7, 0x1fc0
	s_add_i32 s6, s60, s6
	v_lshlrev_b32_e32 v144, 2, v4
	v_xad_u32 v166, v13, v164, 0
	v_xad_u32 v170, v14, v13, 0
	s_sub_i32 s65, s7, 64
	v_add_u32_e32 v13, s6, v145
	s_lshl_b32 s6, s46, 18
	v_ashrrev_i32_e32 v147, 31, v146
	v_sub_u32_e32 v13, v13, v144
	s_add_u32 s6, s90, s6
	v_lshl_add_u64 v[148:149], v[146:147], 2, s[38:39]
	v_subrev_u32_e32 v147, s7, v13
	s_addc_u32 s7, s91, 0
	v_add_u32_e32 v0, v0, v10
	v_lshl_add_u64 v[150:151], s[6:7], 0, v[0:1]
	v_add3_u32 v0, s61, v6, v11
	v_lshl_add_u64 v[152:153], s[6:7], 0, v[0:1]
	v_add_u32_e32 v0, v7, v5
	v_add3_u32 v0, v0, v8, v2
	v_lshl_or_b32 v0, v0, 12, v9
	v_add_u32_e32 v0, v0, v3
	v_lshl_add_u64 v[154:155], s[6:7], 0, v[0:1]
	v_add_u32_e32 v0, s62, v4
	v_lshlrev_b32_e32 v4, 1, v0
	s_mov_b32 s38, 0xffff0
	v_and_or_b32 v4, v4, s38, v5
	v_and_b32_e32 v0, 4, v0
	v_add_u32_e32 v162, s4, v12
	v_lshrrev_b32_e32 v12, 5, v146
	v_add_u32_e32 v0, v4, v0
	v_add_lshl_u32 v0, v0, v2, 12
	v_add_u16_e32 v2, 2, v12
	v_and_b32_e32 v2, 3, v2
	v_lshlrev_b32_e32 v2, 6, v2
	s_waitcnt vmcnt(0)
	v_or3_b32 v0, v0, v2, v3
	v_mov_b32_e32 v14, v1
	v_mov_b32_e32 v15, v1
	v_lshl_add_u64 v[156:157], s[6:7], 0, v[0:1]
	v_mov_b32_e32 v0, v1
	v_mov_b32_e32 v2, v1
	v_mov_b32_e32 v3, v1
	v_mov_b32_e32 v4, v1
	v_mov_b32_e32 v5, v1
	v_mov_b32_e32 v6, v1
	v_mov_b32_e32 v7, v1
	v_mov_b32_e32 v8, v1
	v_mov_b32_e32 v9, v1
	v_mov_b32_e32 v10, v1
	v_mov_b32_e32 v11, v1
	v_mov_b32_e32 v12, v1
	v_mov_b32_e32 v13, v1
	s_waitcnt lgkmcnt(0)
	v_mov_b64_e32 v[30:31], v[14:15]
	v_mov_b64_e32 v[46:47], v[14:15]
	v_mov_b64_e32 v[62:63], v[14:15]
	v_mov_b64_e32 v[78:79], v[14:15]
	s_mov_b32 s45, 0
	v_lshlrev_b32_e32 v165, 8, v145
	v_cmp_gt_u32_e64 s[4:5], 32, v146
	v_lshl_add_u32 v167, v145, 2, s54
	v_add_u32_e32 v161, s54, v164
	v_mov_b32_e32 v174, 0
	v_mov_b32_e32 v173, 0xf149f2ca
	s_mov_b32 s66, s46
	v_mov_b64_e32 v[28:29], v[12:13]
	v_mov_b64_e32 v[26:27], v[10:11]
	v_mov_b64_e32 v[24:25], v[8:9]
	v_mov_b64_e32 v[22:23], v[6:7]
	v_mov_b64_e32 v[20:21], v[4:5]
	v_mov_b64_e32 v[18:19], v[2:3]
	v_mov_b64_e32 v[16:17], v[0:1]
	v_mov_b64_e32 v[44:45], v[12:13]
	v_mov_b64_e32 v[42:43], v[10:11]
	v_mov_b64_e32 v[40:41], v[8:9]
	v_mov_b64_e32 v[38:39], v[6:7]
	v_mov_b64_e32 v[36:37], v[4:5]
	v_mov_b64_e32 v[34:35], v[2:3]
	v_mov_b64_e32 v[32:33], v[0:1]
	v_mov_b64_e32 v[60:61], v[12:13]
	v_mov_b64_e32 v[58:59], v[10:11]
	v_mov_b64_e32 v[56:57], v[8:9]
	v_mov_b64_e32 v[54:55], v[6:7]
	v_mov_b64_e32 v[52:53], v[4:5]
	v_mov_b64_e32 v[50:51], v[2:3]
	v_mov_b64_e32 v[48:49], v[0:1]
	v_mov_b64_e32 v[76:77], v[12:13]
	v_mov_b64_e32 v[74:75], v[10:11]
	v_mov_b64_e32 v[72:73], v[8:9]
	v_mov_b64_e32 v[70:71], v[6:7]
	v_mov_b64_e32 v[68:69], v[4:5]
	v_mov_b64_e32 v[66:67], v[2:3]
	v_mov_b64_e32 v[64:65], v[0:1]
	s_waitcnt vmcnt(0)
	s_barrier
	s_mov_b32 s45, 0
	s_lshl_b32 s65, s46, 6
	s_mov_b32 s66, 0
	s_mov_b32 s33, 0x8000
	s_mov_b32 s42, 0xc000
	s_mov_b32 s43, 0x11000
	s_mov_b32 s47, 0x10800
	s_mov_b32 s100, 0x10900
	s_mov_b32 s101, 0x10a00
	v_subrev_u32_e32 v147, 64, v147
	v_lshlrev_b32_e32 v232, 2, v146
	s_lshr_b32 s6, s68, 11
	s_and_b32 s7, s6, 3
	s_lshl_b32 s98, s7, 12
	s_lshl_b32 s99, s7, 16
	s_add_i32 s40, s46, -1
	s_lshl_b32 s41, s40, 8
	s_lshl_b32 s39, s40, 18
	s_add_u32 s40, s30, s41
	s_addc_u32 s41, s31, 0
	s_add_u32 s39, s39, s99
	s_cmp_ge_u32 s6, 4
	s_cbranch_scc1 .Lat_setup_b
	s_add_u32 s38, s82, s39
	s_addc_u32 s39, s83, 0
	v_lshrrev_b32_e32 v0, 4, v146
	v_and_b32_e32 v2, 15, v146
	v_xor_b32_e32 v2, v2, v0
	v_lshlrev_b32_e32 v2, 4, v2
	v_lshl_add_u32 v228, v0, 12, v2
	v_xor_b32_e32 v229, 64, v228
	v_add_u32_e32 v229, 0x4000, v229
	v_add_u32_e32 v230, 0x8000, v228
	v_xor_b32_e32 v231, 64, v228
	v_add_u32_e32 v231, 0xc000, v231
	s_add_i32 s6, s42, s98
	s_mov_b32 s7, s6
	s_mov_b32 m0, s7
	s_add_i32 s7, s7, 0x400
	global_load_lds_dwordx4 v228, s[38:39]
	s_mov_b32 m0, s7
	s_add_i32 s7, s7, 0x400
	global_load_lds_dwordx4 v229, s[38:39]
	s_mov_b32 m0, s7
	s_add_i32 s7, s7, 0x400
	global_load_lds_dwordx4 v230, s[38:39]
	s_mov_b32 m0, s7
	s_nop 0
	global_load_lds_dwordx4 v231, s[38:39]
	global_load_dword v154, v232, s[40:41]
	s_sub_u32 s38, s38, 0x40000
	s_subb_u32 s39, s39, 0
	s_sub_u32 s40, s40, 0x100
	s_subb_u32 s41, s41, 0
	s_branch .Lat_setup_done
.Lat_setup_b:
	s_add_u32 s38, s84, s39
	s_addc_u32 s39, s85, 0
	v_bfe_u32 v0, v146, 4, 1
	v_bfe_u32 v2, v146, 2, 2
	v_lshl_add_u32 v0, v0, 3, v2
	v_lshlrev_b32_e32 v0, 12, v0
	v_lshrrev_b32_e32 v2, 5, v146
	v_lshl_add_u32 v0, v2, 6, v0
	v_and_b32_e32 v2, 3, v146
	v_lshl_add_u32 v228, v2, 4, v0
	v_add_u32_e32 v229, 0x80, v228
	v_add_u32_e32 v230, 0x4000, v228
	v_add_u32_e32 v231, 0x4080, v228
.Lat_setup_done:
	s_cmp_gt_i32 s65, s64
	s_cbranch_scc1 .Lat_pre0_skip
	v_add3_u32 v0, v166, v165, s33
	v_add3_u32 v14, v168, v165, s33
	v_add3_u32 v15, v169, v165, s33
	v_add3_u32 v175, v170, v165, s33
	ds_read_b128 v[2:5], v0
	ds_read_b128 v[6:9], v0 offset:128
	ds_read_b128 v[10:13], v0 offset:8192
	ds_read_b128 v[176:179], v0 offset:8320
	ds_read_b128 v[180:183], v14
	ds_read_b128 v[184:187], v14 offset:128
	ds_read_b128 v[188:191], v14 offset:8192
	ds_read_b128 v[192:195], v14 offset:8320
	ds_read_b128 v[196:199], v15
	ds_read_b128 v[200:203], v15 offset:128
	ds_read_b128 v[204:207], v15 offset:8192
	ds_read_b128 v[208:211], v15 offset:8320
	ds_read_b128 v[212:215], v175
	ds_read_b128 v[216:219], v175 offset:128
	ds_read_b128 v[220:223], v175 offset:8192
	ds_read_b128 v[224:227], v175 offset:8320
	v_add_u32_e32 v0, s47, v164
	ds_read_b128 v[96:99], v0
	ds_read_b128 v[100:103], v0 offset:32
	ds_read_b128 v[80:83], v0 offset:128
	ds_read_b128 v[84:87], v0 offset:160
	ds_read_b128 v[104:107], v0 offset:64
	ds_read_b128 v[108:111], v0 offset:96
	ds_read_b128 v[88:91], v0 offset:192
	ds_read_b128 v[92:95], v0 offset:224
.Lat_pre0_skip:
	s_cmp_ge_u32 s68, 0x2000
	s_cbranch_scc0 .Lat_tile
	s_barrier
.Lat_tile:
	s_cmp_ge_u32 s68, 0x2000
	s_cbranch_scc1 .Lat_dma_b
	s_add_i32 s6, s45, 2
	s_cmp_ge_u32 s6, s46
	s_cbranch_scc1 .Lat_nodma
	s_add_i32 s6, s43, s98
	s_mov_b32 s7, s6
	s_mov_b32 m0, s7
	s_add_i32 s7, s7, 0x400
	global_load_lds_dwordx4 v228, s[38:39]
	s_mov_b32 m0, s7
	s_add_i32 s7, s7, 0x400
	global_load_lds_dwordx4 v229, s[38:39]
	s_mov_b32 m0, s7
	s_add_i32 s7, s7, 0x400
	global_load_lds_dwordx4 v230, s[38:39]
	s_mov_b32 m0, s7
	s_nop 0
	global_load_lds_dwordx4 v231, s[38:39]
	global_load_dword v172, v232, s[40:41]
	s_branch .Lat_nodma
.Lat_dma_b:
	s_add_i32 s6, s45, 1
	s_cmp_ge_u32 s6, s46
	s_cbranch_scc1 .Lat_nodma
	s_xor_b32 s6, s66, 0x4000
	s_add_i32 s6, s6, s98
	s_mov_b32 s7, s6
	s_mov_b32 m0, s7
	s_add_i32 s7, s7, 0x400
	global_load_lds_dwordx4 v228, s[38:39]
	s_mov_b32 m0, s7
	s_add_i32 s7, s7, 0x400
	global_load_lds_dwordx4 v229, s[38:39]
	s_mov_b32 m0, s7
	s_add_i32 s7, s7, 0x400
	global_load_lds_dwordx4 v230, s[38:39]
	s_mov_b32 m0, s7
	s_nop 0
	global_load_lds_dwordx4 v231, s[38:39]
.Lat_nodma:
	s_cmp_gt_i32 s65, s64
	s_cbranch_scc1 .Lat_skip1
	s_waitcnt lgkmcnt(0)
	v_mfma_f32_32x32x16_bf16 v[96:111], v[2:5], v[112:115], v[96:111]
	v_mfma_f32_32x32x16_bf16 v[80:95], v[10:13], v[112:115], v[80:95]
	v_mfma_f32_32x32x16_bf16 v[96:111], v[180:183], v[116:119], v[96:111]
	v_mfma_f32_32x32x16_bf16 v[80:95], v[188:191], v[116:119], v[80:95]
	v_mfma_f32_32x32x16_bf16 v[96:111], v[196:199], v[120:123], v[96:111]
	v_mfma_f32_32x32x16_bf16 v[80:95], v[204:207], v[120:123], v[80:95]
	v_mfma_f32_32x32x16_bf16 v[96:111], v[212:215], v[124:127], v[96:111]
	v_mfma_f32_32x32x16_bf16 v[80:95], v[220:223], v[124:127], v[80:95]
	v_mfma_f32_32x32x16_bf16 v[96:111], v[6:9], v[128:131], v[96:111]
	v_mfma_f32_32x32x16_bf16 v[80:95], v[176:179], v[128:131], v[80:95]
	v_mfma_f32_32x32x16_bf16 v[96:111], v[184:187], v[132:135], v[96:111]
	v_mfma_f32_32x32x16_bf16 v[80:95], v[192:195], v[132:135], v[80:95]
	v_mfma_f32_32x32x16_bf16 v[96:111], v[200:203], v[136:139], v[96:111]
	v_mfma_f32_32x32x16_bf16 v[80:95], v[208:211], v[136:139], v[80:95]
	v_mfma_f32_32x32x16_bf16 v[96:111], v[216:219], v[140:143], v[96:111]
	v_mfma_f32_32x32x16_bf16 v[80:95], v[224:227], v[140:143], v[80:95]
	s_add_i32 s6, s65, 63
	s_cmp_gt_i32 s6, s44
	s_cbranch_scc1 .Lat_mask
	s_cmp_lt_i32 s65, 0x70
	s_cbranch_scc0 .Lat_nomask
.Lat_mask:
	s_nop 13
	v_cmp_lt_u32_e32 vcc, v147, v163
	v_subrev_u32_e32 v0, 32, v147
	s_nop 0
	v_cndmask_b32_e32 v96, v160, v96, vcc
	v_cmp_lt_u32_e32 vcc, v0, v163
	v_subrev_u32_e32 v0, 1, v147
	s_nop 0
	v_cndmask_b32_e32 v80, v160, v80, vcc
	v_cmp_lt_u32_e32 vcc, v0, v163
	v_subrev_u32_e32 v0, 33, v147
	s_nop 0
	v_cndmask_b32_e32 v97, v160, v97, vcc
	v_cmp_lt_u32_e32 vcc, v0, v163
	v_subrev_u32_e32 v0, 2, v147
	s_nop 0
	v_cndmask_b32_e32 v81, v160, v81, vcc
	v_cmp_lt_u32_e32 vcc, v0, v163
	v_subrev_u32_e32 v0, 34, v147
	s_nop 0
	v_cndmask_b32_e32 v98, v160, v98, vcc
	v_cmp_lt_u32_e32 vcc, v0, v163
	v_subrev_u32_e32 v0, 3, v147
	s_nop 0
	v_cndmask_b32_e32 v82, v160, v82, vcc
	v_cmp_lt_u32_e32 vcc, v0, v163
	v_subrev_u32_e32 v0, 35, v147
	s_nop 0
	v_cndmask_b32_e32 v99, v160, v99, vcc
	v_cmp_lt_u32_e32 vcc, v0, v163
	v_subrev_u32_e32 v0, 8, v147
	s_nop 0
	v_cndmask_b32_e32 v83, v160, v83, vcc
	v_cmp_lt_u32_e32 vcc, v0, v163
	v_subrev_u32_e32 v0, 40, v147
	s_nop 0
	v_cndmask_b32_e32 v100, v160, v100, vcc
	v_cmp_lt_u32_e32 vcc, v0, v163
	v_subrev_u32_e32 v0, 9, v147
	s_nop 0
	v_cndmask_b32_e32 v84, v160, v84, vcc
	v_cmp_lt_u32_e32 vcc, v0, v163
	v_subrev_u32_e32 v0, 41, v147
	s_nop 0
	v_cndmask_b32_e32 v101, v160, v101, vcc
	v_cmp_lt_u32_e32 vcc, v0, v163
	v_subrev_u32_e32 v0, 10, v147
	s_nop 0
	v_cndmask_b32_e32 v85, v160, v85, vcc
	v_cmp_lt_u32_e32 vcc, v0, v163
	v_subrev_u32_e32 v0, 42, v147
	s_nop 0
	v_cndmask_b32_e32 v102, v160, v102, vcc
	v_cmp_lt_u32_e32 vcc, v0, v163
	v_subrev_u32_e32 v0, 11, v147
	s_nop 0
	v_cndmask_b32_e32 v86, v160, v86, vcc
	v_cmp_lt_u32_e32 vcc, v0, v163
	v_subrev_u32_e32 v0, 43, v147
	s_nop 0
	v_cndmask_b32_e32 v103, v160, v103, vcc
	v_cmp_lt_u32_e32 vcc, v0, v163
	v_subrev_u32_e32 v0, 16, v147
	s_nop 0
	v_cndmask_b32_e32 v87, v160, v87, vcc
	v_cmp_lt_u32_e32 vcc, v0, v163
	v_subrev_u32_e32 v0, 48, v147
	s_nop 0
	v_cndmask_b32_e32 v104, v160, v104, vcc
	v_cmp_lt_u32_e32 vcc, v0, v163
	v_subrev_u32_e32 v0, 17, v147
	s_nop 0
	v_cndmask_b32_e32 v88, v160, v88, vcc
	v_cmp_lt_u32_e32 vcc, v0, v163
	v_subrev_u32_e32 v0, 49, v147
	s_nop 0
	v_cndmask_b32_e32 v105, v160, v105, vcc
	v_cmp_lt_u32_e32 vcc, v0, v163
	v_subrev_u32_e32 v0, 18, v147
	s_nop 0
	v_cndmask_b32_e32 v89, v160, v89, vcc
	v_cmp_lt_u32_e32 vcc, v0, v163
	v_subrev_u32_e32 v0, 50, v147
	s_nop 0
	v_cndmask_b32_e32 v106, v160, v106, vcc
	v_cmp_lt_u32_e32 vcc, v0, v163
	v_subrev_u32_e32 v0, 19, v147
	s_nop 0
	v_cndmask_b32_e32 v90, v160, v90, vcc
	v_cmp_lt_u32_e32 vcc, v0, v163
	v_subrev_u32_e32 v0, 51, v147
	s_nop 0
	v_cndmask_b32_e32 v107, v160, v107, vcc
	v_cmp_lt_u32_e32 vcc, v0, v163
	v_subrev_u32_e32 v0, 24, v147
	s_nop 0
	v_cndmask_b32_e32 v91, v160, v91, vcc
	v_cmp_lt_u32_e32 vcc, v0, v163
	v_subrev_u32_e32 v0, 56, v147
	s_nop 0
	v_cndmask_b32_e32 v108, v160, v108, vcc
	v_cmp_lt_u32_e32 vcc, v0, v163
	v_subrev_u32_e32 v0, 25, v147
	s_nop 0
	v_cndmask_b32_e32 v92, v160, v92, vcc
	v_cmp_lt_u32_e32 vcc, v0, v163
	v_subrev_u32_e32 v0, 57, v147
	s_nop 0
	v_cndmask_b32_e32 v109, v160, v109, vcc
	v_cmp_lt_u32_e32 vcc, v0, v163
	v_subrev_u32_e32 v0, 26, v147
	s_nop 0
	v_cndmask_b32_e32 v93, v160, v93, vcc
	v_cmp_lt_u32_e32 vcc, v0, v163
	v_subrev_u32_e32 v0, 58, v147
	s_nop 0
	v_cndmask_b32_e32 v110, v160, v110, vcc
	v_cmp_lt_u32_e32 vcc, v0, v163
	v_subrev_u32_e32 v0, 27, v147
	s_nop 0
	v_cndmask_b32_e32 v94, v160, v94, vcc
	v_cmp_lt_u32_e32 vcc, v0, v163
	v_subrev_u32_e32 v0, 59, v147
	s_nop 0
	v_cndmask_b32_e32 v111, v160, v111, vcc
	v_cmp_lt_u32_e32 vcc, v0, v163
	s_nop 0
	s_nop 0
	v_cndmask_b32_e32 v95, v160, v95, vcc
.Lat_nomask:
	s_nop 13
	v_max_f32_e32 v0, v97, v97
	v_max_f32_e32 v2, v96, v96
	v_max_f32_e32 v0, v2, v0
	v_max3_f32 v0, v0, v98, v99
	v_max3_f32 v0, v0, v100, v101
	v_max3_f32 v0, v0, v102, v103
	v_max3_f32 v0, v0, v104, v105
	v_max3_f32 v0, v0, v106, v107
	v_max3_f32 v0, v0, v108, v109
	v_max3_f32 v0, v0, v110, v111
	v_max3_f32 v0, v0, v80, v81
	v_max3_f32 v0, v0, v82, v83
	v_max3_f32 v0, v0, v84, v85
	v_max3_f32 v0, v0, v86, v87
	v_max3_f32 v0, v0, v88, v89
	v_max3_f32 v0, v0, v90, v91
	v_max3_f32 v0, v0, v92, v93
	v_max3_f32 v0, v0, v94, v95
	v_mov_b32_e32 v2, v0
	s_nop 1
	v_permlane32_swap_b32_e32 v0, v2
	v_max_f32_e32 v2, v2, v2
	v_max_f32_e32 v0, v0, v0
	v_max_f32_e32 v0, v0, v2
	v_sub_f32_e32 v2, v0, v173
	v_mul_f32_e32 v2, 0x3db504f3, v2
	v_cmp_ge_f32_e32 vcc, s63, v2
	v_max_f32_e32 v2, v173, v173
	v_max_f32_e32 v2, v2, v0
	v_sub_f32_e32 v0, v173, v2
	v_mul_f32_e32 v0, 0x3e0293ee, v0
	v_exp_f32_e32 v0, v0
	s_cmp_eq_u64 vcc, exec
	s_cselect_b64 s[6:7], -1, 0
	v_cndmask_b32_e64 v0, v0, 1.0, s[6:7]
	v_cmp_gt_f32_e32 vcc, 1.0, v0
	v_mov_b32_e32 v233, v0
	s_cbranch_vccz .Lat_norescale
	s_and_saveexec_b64 vcc, s[4:5]
	ds_write_b32 v167, v0 offset:128
	s_or_b64 exec, exec, vcc
	s_waitcnt lgkmcnt(0)
	ds_read_b128 v[4:7], v161 offset:224
	ds_read_b128 v[8:11], v161 offset:192
	ds_read_b128 v[12:15], v161 offset:160
	ds_read_b128 v[176:179], v161 offset:128
	s_waitcnt lgkmcnt(0)
	v_pk_mul_f32 v[78:79], v[78:79], v[6:7]
	v_pk_mul_f32 v[74:75], v[74:75], v[10:11]
	v_pk_mul_f32 v[70:71], v[70:71], v[14:15]
	v_pk_mul_f32 v[66:67], v[66:67], v[178:179]
	v_pk_mul_f32 v[76:77], v[76:77], v[4:5]
	v_pk_mul_f32 v[72:73], v[72:73], v[8:9]
	v_pk_mul_f32 v[68:69], v[68:69], v[12:13]
	v_pk_mul_f32 v[64:65], v[64:65], v[176:177]
	v_pk_mul_f32 v[62:63], v[62:63], v[6:7]
	v_pk_mul_f32 v[58:59], v[58:59], v[10:11]
	v_pk_mul_f32 v[54:55], v[54:55], v[14:15]
	v_pk_mul_f32 v[50:51], v[50:51], v[178:179]
	v_pk_mul_f32 v[60:61], v[60:61], v[4:5]
	v_pk_mul_f32 v[56:57], v[56:57], v[8:9]
	v_pk_mul_f32 v[52:53], v[52:53], v[12:13]
	v_pk_mul_f32 v[48:49], v[48:49], v[176:177]
	v_pk_mul_f32 v[46:47], v[46:47], v[6:7]
	v_pk_mul_f32 v[42:43], v[42:43], v[10:11]
	v_pk_mul_f32 v[38:39], v[38:39], v[14:15]
	v_pk_mul_f32 v[34:35], v[34:35], v[178:179]
	v_pk_mul_f32 v[44:45], v[44:45], v[4:5]
	v_pk_mul_f32 v[40:41], v[40:41], v[8:9]
	v_pk_mul_f32 v[36:37], v[36:37], v[12:13]
	v_pk_mul_f32 v[32:33], v[32:33], v[176:177]
	v_pk_mul_f32 v[30:31], v[30:31], v[6:7]
	v_pk_mul_f32 v[26:27], v[26:27], v[10:11]
	v_pk_mul_f32 v[22:23], v[22:23], v[14:15]
	v_pk_mul_f32 v[18:19], v[18:19], v[178:179]
	v_pk_mul_f32 v[28:29], v[28:29], v[4:5]
	v_pk_mul_f32 v[24:25], v[24:25], v[8:9]
	v_pk_mul_f32 v[20:21], v[20:21], v[12:13]
	v_pk_mul_f32 v[16:17], v[16:17], v[176:177]
.Lat_norescale:
	v_cndmask_b32_e64 v173, v2, v173, s[6:7]
	v_mul_f32_e32 v2, 0xbe0293ee, v173
	v_fmamk_f32 v96, v96, 0x3e0293ee, v2
	v_fmamk_f32 v97, v97, 0x3e0293ee, v2
	v_fmamk_f32 v98, v98, 0x3e0293ee, v2
	v_fmamk_f32 v99, v99, 0x3e0293ee, v2
	v_fmamk_f32 v100, v100, 0x3e0293ee, v2
	v_fmamk_f32 v101, v101, 0x3e0293ee, v2
	v_fmamk_f32 v102, v102, 0x3e0293ee, v2
	v_fmamk_f32 v103, v103, 0x3e0293ee, v2
	v_fmamk_f32 v104, v104, 0x3e0293ee, v2
	v_fmamk_f32 v105, v105, 0x3e0293ee, v2
	v_fmamk_f32 v106, v106, 0x3e0293ee, v2
	v_fmamk_f32 v107, v107, 0x3e0293ee, v2
	v_fmamk_f32 v108, v108, 0x3e0293ee, v2
	v_fmamk_f32 v109, v109, 0x3e0293ee, v2
	v_fmamk_f32 v110, v110, 0x3e0293ee, v2
	v_fmamk_f32 v111, v111, 0x3e0293ee, v2
	v_fmamk_f32 v80, v80, 0x3e0293ee, v2
	v_fmamk_f32 v81, v81, 0x3e0293ee, v2
	v_fmamk_f32 v82, v82, 0x3e0293ee, v2
	v_fmamk_f32 v83, v83, 0x3e0293ee, v2
	v_fmamk_f32 v84, v84, 0x3e0293ee, v2
	v_fmamk_f32 v85, v85, 0x3e0293ee, v2
	v_fmamk_f32 v86, v86, 0x3e0293ee, v2
	v_fmamk_f32 v87, v87, 0x3e0293ee, v2
	v_fmamk_f32 v88, v88, 0x3e0293ee, v2
	v_fmamk_f32 v89, v89, 0x3e0293ee, v2
	v_fmamk_f32 v90, v90, 0x3e0293ee, v2
	v_fmamk_f32 v91, v91, 0x3e0293ee, v2
	v_fmamk_f32 v92, v92, 0x3e0293ee, v2
	v_fmamk_f32 v93, v93, 0x3e0293ee, v2
	v_fmamk_f32 v94, v94, 0x3e0293ee, v2
	v_fmamk_f32 v95, v95, 0x3e0293ee, v2
	v_exp_f32_e32 v96, v96
	v_exp_f32_e32 v97, v97
	v_exp_f32_e32 v98, v98
	v_exp_f32_e32 v99, v99
	v_exp_f32_e32 v100, v100
	v_exp_f32_e32 v101, v101
	v_exp_f32_e32 v102, v102
	v_exp_f32_e32 v103, v103
	v_exp_f32_e32 v104, v104
	v_exp_f32_e32 v105, v105
	v_exp_f32_e32 v106, v106
	v_exp_f32_e32 v107, v107
	v_exp_f32_e32 v108, v108
	v_exp_f32_e32 v109, v109
	v_exp_f32_e32 v110, v110
	v_exp_f32_e32 v111, v111
.Lat_skip1:
	s_cmp_lg_u32 s45, 0
	s_cbranch_scc1 .Lat_not_first
	s_waitcnt vmcnt(5)
	s_and_b64 vcc, exec, s[2:3]
	s_cbranch_vccnz .Lat_not_first
	v_add_u32_e32 v0, 0x100, v171
	ds_write_b32 v0, v154
	s_waitcnt lgkmcnt(0)
.Lat_not_first:
	s_barrier
	s_cmp_gt_i32 s65, s64
	s_cselect_b32 s6, 0, 1
	s_cmp_eq_u32 s6, 0
	s_cbranch_scc1 .Lat_nov0
	v_add_u32_e32 v153, s66, v162
	ds_read_b64_tr_b16 v[2:3], v153 offset:0
	ds_read_b64_tr_b16 v[4:5], v153 offset:2048
	ds_read_b64_tr_b16 v[10:11], v153 offset:4096
	ds_read_b64_tr_b16 v[12:13], v153 offset:6144
	ds_read_b64_tr_b16 v[180:181], v153 offset:8192
	ds_read_b64_tr_b16 v[182:183], v153 offset:10240
	ds_read_b64_tr_b16 v[188:189], v153 offset:12288
	ds_read_b64_tr_b16 v[190:191], v153 offset:14336
	ds_read_b64_tr_b16 v[196:197], v153 offset:512
	ds_read_b64_tr_b16 v[198:199], v153 offset:2560
	ds_read_b64_tr_b16 v[204:205], v153 offset:4608
	ds_read_b64_tr_b16 v[206:207], v153 offset:6656
	ds_read_b64_tr_b16 v[212:213], v153 offset:8704
	ds_read_b64_tr_b16 v[214:215], v153 offset:10752
	ds_read_b64_tr_b16 v[220:221], v153 offset:12800
	ds_read_b64_tr_b16 v[222:223], v153 offset:14848
	ds_read_b64_tr_b16 v[6:7], v153 offset:1024
	ds_read_b64_tr_b16 v[8:9], v153 offset:3072
	ds_read_b64_tr_b16 v[176:177], v153 offset:5120
	ds_read_b64_tr_b16 v[178:179], v153 offset:7168
	ds_read_b64_tr_b16 v[184:185], v153 offset:9216
	ds_read_b64_tr_b16 v[186:187], v153 offset:11264
	ds_read_b64_tr_b16 v[192:193], v153 offset:13312
	ds_read_b64_tr_b16 v[194:195], v153 offset:15360
	ds_read_b64_tr_b16 v[200:201], v153 offset:1536
	ds_read_b64_tr_b16 v[202:203], v153 offset:3584
	ds_read_b64_tr_b16 v[208:209], v153 offset:5632
	ds_read_b64_tr_b16 v[210:211], v153 offset:7680
	ds_read_b64_tr_b16 v[216:217], v153 offset:9728
	ds_read_b64_tr_b16 v[218:219], v153 offset:11776
	ds_read_b64_tr_b16 v[224:225], v153 offset:13824
	ds_read_b64_tr_b16 v[226:227], v153 offset:15872
.Lat_nov0:
	v_add3_u32 v0, v166, v165, s42
	v_add3_u32 v14, v168, v165, s42
	v_add3_u32 v15, v169, v165, s42
	v_add3_u32 v175, v170, v165, s42
	s_mov_b32 s99, 0
	s_add_i32 s7, s45, 1
	s_cmp_ge_u32 s7, s46
	s_cbranch_scc1 .Lat_nokpre
	s_add_i32 s7, s65, 0xffffffc0
	s_cmp_gt_i32 s7, s64
	s_cbranch_scc1 .Lat_nokpre
	s_mov_b32 s99, 1
.Lat_nokpre:
	s_cmp_eq_u32 s6, 0
	s_cbranch_scc1 .Lat_skip2
	v_exp_f32_e32 v80, v80
	v_exp_f32_e32 v81, v81
	v_exp_f32_e32 v82, v82
	v_exp_f32_e32 v83, v83
	v_exp_f32_e32 v84, v84
	v_exp_f32_e32 v85, v85
	v_exp_f32_e32 v86, v86
	v_exp_f32_e32 v87, v87
	v_exp_f32_e32 v88, v88
	v_exp_f32_e32 v89, v89
	v_exp_f32_e32 v90, v90
	v_exp_f32_e32 v91, v91
	v_exp_f32_e32 v92, v92
	v_exp_f32_e32 v93, v93
	v_exp_f32_e32 v94, v94
	v_exp_f32_e32 v95, v95
	v_add_f32_e32 v148, v96, v100
	v_add_f32_e32 v149, v97, v101
	v_add_f32_e32 v150, v98, v102
	v_add_f32_e32 v151, v99, v103
	v_add_f32_e32 v148, v148, v104
	v_add_f32_e32 v149, v149, v105
	v_add_f32_e32 v150, v150, v106
	v_add_f32_e32 v151, v151, v107
	v_add_f32_e32 v148, v148, v108
	v_add_f32_e32 v149, v149, v109
	v_add_f32_e32 v150, v150, v110
	v_add_f32_e32 v151, v151, v111
	v_add_f32_e32 v148, v148, v80
	v_add_f32_e32 v149, v149, v81
	v_add_f32_e32 v150, v150, v82
	v_add_f32_e32 v151, v151, v83
	v_add_f32_e32 v148, v148, v84
	v_add_f32_e32 v149, v149, v85
	v_add_f32_e32 v150, v150, v86
	v_add_f32_e32 v151, v151, v87
	v_add_f32_e32 v148, v148, v88
	v_add_f32_e32 v149, v149, v89
	v_add_f32_e32 v150, v150, v90
	v_add_f32_e32 v151, v151, v91
	v_add_f32_e32 v148, v148, v92
	v_add_f32_e32 v149, v149, v93
	v_add_f32_e32 v150, v150, v94
	v_add_f32_e32 v151, v151, v95
	v_add_f32_e32 v148, v148, v149
	v_add_f32_e32 v150, v150, v151
	v_add_f32_e32 v148, v148, v150
	v_mov_b32_e32 v152, v148
	s_nop 1
	v_permlane32_swap_b32_e32 v148, v152
	v_add_f32_e32 v148, v148, v152
	v_fma_f32 v174, v174, v233, v148
	v_cvt_pk_bf16_f32 v96, v96, v97
	v_cvt_pk_bf16_f32 v97, v98, v99
	v_cvt_pk_bf16_f32 v98, v100, v101
	v_cvt_pk_bf16_f32 v99, v102, v103
	v_cvt_pk_bf16_f32 v100, v104, v105
	v_cvt_pk_bf16_f32 v101, v106, v107
	v_cvt_pk_bf16_f32 v102, v108, v109
	v_cvt_pk_bf16_f32 v103, v110, v111
	v_cvt_pk_bf16_f32 v104, v80, v81
	v_cvt_pk_bf16_f32 v105, v82, v83
	v_cvt_pk_bf16_f32 v106, v84, v85
	v_cvt_pk_bf16_f32 v107, v86, v87
	v_cvt_pk_bf16_f32 v108, v88, v89
	v_cvt_pk_bf16_f32 v109, v90, v91
	v_cvt_pk_bf16_f32 v110, v92, v93
	v_cvt_pk_bf16_f32 v111, v94, v95
	s_nop 1
	v_permlane32_swap_b32_e32 v96, v98
	v_permlane32_swap_b32_e32 v97, v99
	v_permlane32_swap_b32_e32 v100, v102
	v_permlane32_swap_b32_e32 v101, v103
	v_permlane32_swap_b32_e32 v104, v106
	v_permlane32_swap_b32_e32 v105, v107
	v_permlane32_swap_b32_e32 v108, v110
	v_permlane32_swap_b32_e32 v109, v111
	s_waitcnt lgkmcnt(0)
	s_cmp_eq_u32 s99, 0
	s_cbranch_scc1 .Lat_pv_nok
	v_mfma_f32_32x32x16_bf16 v[64:79], v[96:99], v[2:5], v[64:79]
	ds_read_b128 v[2:5], v0
	v_mfma_f32_32x32x16_bf16 v[64:79], v[100:103], v[10:13], v[64:79]
	ds_read_b128 v[10:13], v0 offset:8192
	v_mfma_f32_32x32x16_bf16 v[64:79], v[104:107], v[180:183], v[64:79]
	ds_read_b128 v[180:183], v14
	v_mfma_f32_32x32x16_bf16 v[64:79], v[108:111], v[188:191], v[64:79]
	ds_read_b128 v[188:191], v14 offset:8192
	v_mfma_f32_32x32x16_bf16 v[48:63], v[96:99], v[196:199], v[48:63]
	ds_read_b128 v[196:199], v15
	v_mfma_f32_32x32x16_bf16 v[48:63], v[100:103], v[204:207], v[48:63]
	ds_read_b128 v[204:207], v15 offset:8192
	v_mfma_f32_32x32x16_bf16 v[48:63], v[104:107], v[212:215], v[48:63]
	ds_read_b128 v[212:215], v175
	v_mfma_f32_32x32x16_bf16 v[48:63], v[108:111], v[220:223], v[48:63]
	ds_read_b128 v[220:223], v175 offset:8192
	v_mfma_f32_32x32x16_bf16 v[32:47], v[96:99], v[6:9], v[32:47]
	ds_read_b128 v[6:9], v0 offset:128
	v_mfma_f32_32x32x16_bf16 v[32:47], v[100:103], v[176:179], v[32:47]
	ds_read_b128 v[176:179], v0 offset:8320
	v_mfma_f32_32x32x16_bf16 v[32:47], v[104:107], v[184:187], v[32:47]
	ds_read_b128 v[184:187], v14 offset:128
	v_mfma_f32_32x32x16_bf16 v[32:47], v[108:111], v[192:195], v[32:47]
	ds_read_b128 v[192:195], v14 offset:8320
	v_mfma_f32_32x32x16_bf16 v[16:31], v[96:99], v[200:203], v[16:31]
	ds_read_b128 v[200:203], v15 offset:128
	v_mfma_f32_32x32x16_bf16 v[16:31], v[100:103], v[208:211], v[16:31]
	ds_read_b128 v[208:211], v15 offset:8320
	v_mfma_f32_32x32x16_bf16 v[16:31], v[104:107], v[216:219], v[16:31]
	ds_read_b128 v[216:219], v175 offset:128
	v_mfma_f32_32x32x16_bf16 v[16:31], v[108:111], v[224:227], v[16:31]
	ds_read_b128 v[224:227], v175 offset:8320
	s_branch .Lat_skip2
.Lat_pv_nok:
	v_mfma_f32_32x32x16_bf16 v[64:79], v[96:99], v[2:5], v[64:79]
	v_mfma_f32_32x32x16_bf16 v[64:79], v[100:103], v[10:13], v[64:79]
	v_mfma_f32_32x32x16_bf16 v[64:79], v[104:107], v[180:183], v[64:79]
	v_mfma_f32_32x32x16_bf16 v[64:79], v[108:111], v[188:191], v[64:79]
	v_mfma_f32_32x32x16_bf16 v[48:63], v[96:99], v[196:199], v[48:63]
	v_mfma_f32_32x32x16_bf16 v[48:63], v[100:103], v[204:207], v[48:63]
	v_mfma_f32_32x32x16_bf16 v[48:63], v[104:107], v[212:215], v[48:63]
	v_mfma_f32_32x32x16_bf16 v[48:63], v[108:111], v[220:223], v[48:63]
	v_mfma_f32_32x32x16_bf16 v[32:47], v[96:99], v[6:9], v[32:47]
	v_mfma_f32_32x32x16_bf16 v[32:47], v[100:103], v[176:179], v[32:47]
	v_mfma_f32_32x32x16_bf16 v[32:47], v[104:107], v[184:187], v[32:47]
	v_mfma_f32_32x32x16_bf16 v[32:47], v[108:111], v[192:195], v[32:47]
	v_mfma_f32_32x32x16_bf16 v[16:31], v[96:99], v[200:203], v[16:31]
	v_mfma_f32_32x32x16_bf16 v[16:31], v[100:103], v[208:211], v[16:31]
	v_mfma_f32_32x32x16_bf16 v[16:31], v[104:107], v[216:219], v[16:31]
	v_mfma_f32_32x32x16_bf16 v[16:31], v[108:111], v[224:227], v[16:31]
	s_branch .Lat_skip2b
.Lat_skip2:
	s_cmp_eq_u32 s6, 1
	s_cbranch_scc1 .Lat_skip2b
	s_cmp_eq_u32 s99, 0
	s_cbranch_scc1 .Lat_skip2b
	ds_read_b128 v[2:5], v0
	ds_read_b128 v[10:13], v0 offset:8192
	ds_read_b128 v[180:183], v14
	ds_read_b128 v[188:191], v14 offset:8192
	ds_read_b128 v[196:199], v15
	ds_read_b128 v[204:207], v15 offset:8192
	ds_read_b128 v[212:215], v175
	ds_read_b128 v[220:223], v175 offset:8192
	ds_read_b128 v[6:9], v0 offset:128
	ds_read_b128 v[176:179], v0 offset:8320
	ds_read_b128 v[184:187], v14 offset:128
	ds_read_b128 v[192:195], v14 offset:8320
	ds_read_b128 v[200:203], v15 offset:128
	ds_read_b128 v[208:211], v15 offset:8320
	ds_read_b128 v[216:219], v175 offset:128
	ds_read_b128 v[224:227], v175 offset:8320
.Lat_skip2b:
	s_add_i32 s7, s45, 1
	s_cmp_ge_u32 s7, s46
	s_cbranch_scc1 .Lat_nockpre
	s_add_i32 s7, s65, 0xffffffc0
	s_cmp_gt_i32 s7, s64
	s_cbranch_scc1 .Lat_nockpre
	v_add_u32_e32 v0, s100, v164
	ds_read_b128 v[96:99], v0
	ds_read_b128 v[100:103], v0 offset:32
	ds_read_b128 v[80:83], v0 offset:128
	ds_read_b128 v[84:87], v0 offset:160
	ds_read_b128 v[104:107], v0 offset:64
	ds_read_b128 v[108:111], v0 offset:96
	ds_read_b128 v[88:91], v0 offset:192
	ds_read_b128 v[92:95], v0 offset:224
.Lat_nockpre:
	s_waitcnt vmcnt(0)
	s_add_i32 s7, s45, 2
	s_cmp_ge_u32 s7, s46
	s_cbranch_scc1 .Lat_nockw
	s_and_b64 vcc, exec, s[2:3]
	s_cbranch_vccnz .Lat_nockw
	s_sub_i32 s7, s101, 0x10800
	v_add_u32_e32 v0, s7, v171
	ds_write_b32 v0, v172
.Lat_nockw:
	s_waitcnt lgkmcnt(0)
	s_barrier
	s_add_i32 s45, s45, 1
	s_addk_i32 s65, 0xffc0
	s_xor_b32 s66, s66, 0x4000
	v_add_u32_e32 v147, 64, v147
	s_sub_u32 s38, s38, 0x40000
	s_subb_u32 s39, s39, 0
	s_sub_u32 s40, s40, 0x100
	s_subb_u32 s41, s41, 0
	s_mov_b32 s7, s33
	s_mov_b32 s33, s42
	s_mov_b32 s42, s43
	s_mov_b32 s43, s7
	s_mov_b32 s7, s47
	s_mov_b32 s47, s100
	s_mov_b32 s100, s101
	s_mov_b32 s101, s7
	s_cmp_lt_u32 s45, s46
	s_cbranch_scc1 .Lat_tile
	s_cmp_ge_u32 s68, 0x2000
	s_cbranch_scc1 .Lat_done
	s_barrier
.Lat_done:
.LBB0_1120:
	s_and_saveexec_b64 s[2:3], s[4:5]
	ds_write_b32 v167, v174
	s_or_b64 exec, exec, s[2:3]
	s_waitcnt lgkmcnt(0)
	ds_read_b32 v3, v161
	v_and_b32_e32 v2, 64, v159
	v_xor_b32_e32 v0, 1, v159
	v_add_u32_e32 v2, 64, v2
	v_cmp_lt_i32_e32 vcc, v0, v2
	s_waitcnt lgkmcnt(0)
	v_rcp_f32_e32 v7, v3
	s_add_u32 s2, s86, s36
	v_cndmask_b32_e32 v0, v159, v0, vcc
	v_lshlrev_b32_e32 v6, 2, v0
	v_mul_f32_e32 v8, v64, v7
	ds_bpermute_b32 v9, v6, v8
	v_and_b32_e32 v0, 1, v146
	s_addc_u32 s3, s87, s37
	v_cmp_eq_u32_e32 vcc, 0, v0
	v_lshlrev_b32_e32 v0, 1, v145
	v_ashrrev_i32_e32 v145, 31, v144
	v_lshl_add_u64 v[2:3], s[2:3], 0, v[0:1]
	v_lshlrev_b64 v[4:5], 12, v[144:145]
	v_lshl_add_u64 v[4:5], v[2:3], 0, v[4:5]
	s_and_saveexec_b64 s[2:3], vcc
	s_cbranch_execz .LBB0_1124
	s_waitcnt lgkmcnt(0)
	v_cvt_pk_bf16_f32 v0, v8, v9
	global_store_dword v[4:5], v0, off

	.amdhsa_kernel _Z6mk_fwd6Params
		.amdhsa_group_segment_fixed_size 0
		.amdhsa_private_segment_fixed_size 0
		.amdhsa_kernarg_size 424
		.amdhsa_user_sgpr_count 2
		.amdhsa_user_sgpr_dispatch_ptr 0
		.amdhsa_user_sgpr_queue_ptr 0
		.amdhsa_user_sgpr_kernarg_segment_ptr 1
		.amdhsa_user_sgpr_dispatch_id 0
		.amdhsa_user_sgpr_kernarg_preload_length 0
		.amdhsa_user_sgpr_kernarg_preload_offset 0
		.amdhsa_user_sgpr_private_segment_size 0
		.amdhsa_uses_dynamic_stack 0
		.amdhsa_enable_private_segment 0
		.amdhsa_system_sgpr_workgroup_id_x 1
		.amdhsa_system_sgpr_workgroup_id_y 0
		.amdhsa_system_sgpr_workgroup_id_z 0
		.amdhsa_system_sgpr_workgroup_info 0
		.amdhsa_system_vgpr_workitem_id 0
		.amdhsa_next_free_vgpr 251
		.amdhsa_next_free_sgpr 102
		.amdhsa_accum_offset 252
		.amdhsa_reserve_vcc 1
		.amdhsa_float_round_mode_32 0
		.amdhsa_float_round_mode_16_64 0
		.amdhsa_float_denorm_mode_32 3
		.amdhsa_float_denorm_mode_16_64 3
		.amdhsa_dx10_clamp 1
		.amdhsa_ieee_mode 1
		.amdhsa_fp16_overflow 0
		.amdhsa_tg_split 0
		.amdhsa_exception_fp_ieee_invalid_op 0
		.amdhsa_exception_fp_denorm_src 0
		.amdhsa_exception_fp_ieee_div_zero 0
		.amdhsa_exception_fp_ieee_overflow 0
		.amdhsa_exception_fp_ieee_underflow 0
		.amdhsa_exception_fp_ieee_inexact 0
		.amdhsa_exception_int_div_zero 0
	.end_amdhsa_kernel

.Lfunc_end0:
	.size	_Z6mk_fwd6Params, .Lfunc_end0-_Z6mk_fwd6Params
	.set _Z6mk_fwd6Params.num_vgpr, 251
	.set _Z6mk_fwd6Params.num_agpr, 0
	.set _Z6mk_fwd6Params.numbered_sgpr, 102
	.set _Z6mk_fwd6Params.num_named_barrier, 0
	.set _Z6mk_fwd6Params.private_seg_size, 0
	.set _Z6mk_fwd6Params.uses_vcc, 1
	.set _Z6mk_fwd6Params.uses_flat_scratch, 0
	.set _Z6mk_fwd6Params.has_dyn_sized_stack, 0
	.set _Z6mk_fwd6Params.has_recursion, 0
	.set _Z6mk_fwd6Params.has_indirect_call, 0

amdhsa.kernels:
  - .agpr_count:     0
    .args:
      - .offset:         0
        .size:           168
        .value_kind:     by_value
      - .offset:         168
        .size:           4
        .value_kind:     hidden_block_count_x
      - .offset:         172
        .size:           4
        .value_kind:     hidden_block_count_y
      - .offset:         176
        .size:           4
        .value_kind:     hidden_block_count_z
      - .offset:         180
        .size:           2
        .value_kind:     hidden_group_size_x
      - .offset:         182
        .size:           2
        .value_kind:     hidden_group_size_y
      - .offset:         184
        .size:           2
        .value_kind:     hidden_group_size_z
      - .offset:         186
        .size:           2
        .value_kind:     hidden_remainder_x
      - .offset:         188
        .size:           2
        .value_kind:     hidden_remainder_y
      - .offset:         190
        .size:           2
        .value_kind:     hidden_remainder_z
      - .offset:         208
        .size:           8
        .value_kind:     hidden_global_offset_x
      - .offset:         216
        .size:           8
        .value_kind:     hidden_global_offset_y
      - .offset:         224
        .size:           8
        .value_kind:     hidden_global_offset_z
      - .offset:         232
        .size:           2
        .value_kind:     hidden_grid_dims
      - .offset:         288
        .size:           4
        .value_kind:     hidden_dynamic_lds_size
    .group_segment_fixed_size: 0
    .kernarg_segment_align: 8
    .kernarg_segment_size: 424
    .language:       OpenCL C
    .language_version:
      - 2
      - 0
    .max_flat_workgroup_size: 512
    .name:           _Z6mk_fwd6Params
    .private_segment_fixed_size: 0
    .sgpr_count:     108
    .sgpr_spill_count: 66
    .symbol:         _Z6mk_fwd6Params.kd
    .uniform_work_group_size: 1
    .uses_dynamic_stack: false
    .vgpr_count:     251
    .vgpr_spill_count: 0
    .wavefront_size: 64
